# XCD-local barriers after phases 4,5,6,10 now also skip the L2 writeback (same-XCD consumers read L2); grouping check cached in a spill lane
# speedup vs baseline: 1.0043x; 1.0013x over previous
_Z6mk_fwd4Args:
	s_load_dword s96, s[0:1], 0xa8
	s_mov_b32 s92, s2
	s_add_u32 s2, s0, 0xa8
	v_writelane_b32 v252, s0, 0
	s_addc_u32 s3, s1, 0
	v_readfirstlane_b32 s33, v0
	v_writelane_b32 v252, s1, 1
	v_writelane_b32 v252, s2, 2
	s_waitcnt lgkmcnt(0)
	s_and_b32 s0, s96, 7
	s_cmp_lg_u32 s0, 0
	v_writelane_b32 v252, s3, 3
	s_mov_b32 s7, 0
	v_writelane_b32 v255, s7, 63
	s_mov_b32 s90, s92
	s_cbranch_scc1 .LBB0_2
	s_ashr_i32 s1, s92, 31
	s_lshr_b32 s1, s1, 29
	s_add_i32 s1, s92, s1
	s_and_b32 s2, s1, -8
	s_ashr_i32 s0, s96, 3
	s_sub_i32 s2, s92, s2
	s_mul_i32 s0, s0, s2
	s_ashr_i32 s1, s1, 3
	s_add_i32 s90, s0, s1

.LBB0_1116:
	s_andn2_saveexec_b64 s[8:9], s[8:9]
	s_cbranch_execz .LBB0_1134
	s_mov_b64 s[8:9], exec
	v_readlane_b32 s10, v255, 63
	s_nop 0
	s_cmp_lg_u32 s10, 0
	s_cbranch_scc1 .Lknown_seam5
	v_mov_b32_e32 v4, 0x8000
	global_load_dwordx2 v[4:5], v4, s[4:5] sc1
	s_waitcnt vmcnt(0)
	v_readfirstlane_b32 s10, v4
	v_readfirstlane_b32 s11, v5
	s_sub_u32 s12, s10, 0x1010101
	s_subb_u32 s13, s11, 0x1010101
	s_and_b64 s[12:13], s[12:13], s[10:11]
	s_cmp_eq_u64 s[12:13], 0
	s_cselect_b32 s10, 2, 1
	v_writelane_b32 v255, s10, 63
.Lknown_seam5:
	s_cmp_eq_u32 s10, 2
	s_cbranch_scc0 .Lfull_seam5
	s_mov_b64 s[4:5], exec
	s_branch .LBB0_1133
.Lfull_seam5:
	buffer_wbl2 sc1
	s_waitcnt lgkmcnt(0)
	s_waitcnt vmcnt(0)
	v_mbcnt_lo_u32_b32 v1, s8, 0
	v_mbcnt_hi_u32_b32 v1, s9, v1
	v_cmp_eq_u32_e32 vcc, 0, v1
	s_and_saveexec_b64 s[10:11], vcc
	s_cbranch_execz .LBB0_1119
	s_bcnt1_i32_b64 s8, s[8:9]
	v_mov_b32_e32 v2, s8
	v_mov_b32_e32 v3, 0x7000
	global_atomic_add v2, v3, v2, s[4:5] offset:1024 sc0

.LBB0_1717:
	s_mov_b64 s[8:9], exec
	v_readlane_b32 s10, v255, 63
	s_nop 0
	s_cmp_lg_u32 s10, 0
	s_cbranch_scc1 .Lknown_seam11
	v_mov_b32_e32 v4, 0x8000
	global_load_dwordx2 v[4:5], v4, s[4:5] sc1
	s_waitcnt vmcnt(0)
	v_readfirstlane_b32 s10, v4
	v_readfirstlane_b32 s11, v5
	s_sub_u32 s12, s10, 0x1010101
	s_subb_u32 s13, s11, 0x1010101
	s_and_b64 s[12:13], s[12:13], s[10:11]
	s_cmp_eq_u64 s[12:13], 0
	s_cselect_b32 s10, 2, 1
	v_writelane_b32 v255, s10, 63
